# v96 + lever 2: GEMM-phase prologue de-serialised (K-tile 1's six LDS-DMA loads issued before the wait for K-tile 0; 13 prologues)
# baseline (speedup 1.0000x reference)
.LBB0_182:
	s_add_u32 s36, s18, 0x6400000
	s_addc_u32 s37, s19, 0
	v_lshl_add_u64 v[10:11], v[0:1], 0, s[56:57]
	s_add_i32 m0, s33, 0x18000
	s_nop 0
	global_load_lds_dwordx4 v[10:11], off
	v_lshl_add_u64 v[10:11], v[0:1], 0, s[0:1]
	s_add_i32 m0, s33, 0x1a000
	s_add_i32 s77, s33, 0x8000
	global_load_lds_dwordx4 v[10:11], off
	v_lshl_add_u64 v[10:11], v[2:3], 0, s[56:57]
	s_mov_b32 m0, s77
	s_add_i32 s78, s33, 0xa000
	global_load_lds_dwordx4 v[10:11], off
	v_lshl_add_u64 v[2:3], v[2:3], 0, s[0:1]
	s_mov_b32 m0, s78
	s_ashr_i32 s42, s39, 31
	global_load_lds_dwordx4 v[2:3], off
	v_lshl_add_u64 v[2:3], v[0:1], 0, s[24:25]
	s_add_i32 m0, s33, 0x1c000
	v_lshl_add_u64 v[0:1], v[0:1], 0, s[26:27]
	global_load_lds_dwordx4 v[2:3], off
	s_add_i32 m0, s33, 0x1e000
	s_lshr_b32 s42, s42, 26
	global_load_lds_dwordx4 v[0:1], off
	s_waitcnt vmcnt(8)
	s_barrier
	v_and_b32_e32 v0, 15, v5
	v_lshlrev_b32_e32 v1, 1, v9
	v_lshl_or_b32 v132, s41, 6, v0
	v_lshl_or_b32 v0, v0, 6, v1
	v_lshlrev_b32_e32 v1, 2, v5
	s_lshl_b32 s40, s40, 5
	s_add_i32 s42, s39, s42
	s_lshl_b32 s41, s41, 13
	v_and_b32_e32 v1, 32, v1
	s_and_b32 s40, s40, 0x60
	s_ashr_i32 s79, s42, 6
	v_bitop3_b32 v2, v0, s41, v1 bitop3:0xde
	s_lshl_b32 s41, s40, 7
	s_cmp_gt_i32 s39, 63
	s_cselect_b64 s[42:43], -1, 0
	s_add_i32 s80, s79, -2
	s_cmpk_lt_u32 s38, 0x100
	s_mov_b32 s38, s46
	v_bitop3_b32 v133, v0, s41, v1 bitop3:0xde
	v_lshlrev_b32_e32 v0, 8, v4
	v_writelane_b32 v253, s38, 54
	s_waitcnt vmcnt(6)
	v_and_b32_e32 v0, 0x18000, v0
	v_lshlrev_b32_e32 v1, 11, v6
	v_writelane_b32 v253, s39, 55
	s_mov_b32 s38, s48
	v_or3_b32 v0, v7, v0, v1
	v_writelane_b32 v253, s38, 56
	s_cselect_b64 s[44:45], -1, 0
	v_or_b32_e32 v134, s40, v9
	v_add_u32_e32 v130, v0, v8
	v_mov_b32_e32 v131, v161
	s_mov_b32 s96, 0
	v_add_u32_e32 v135, 0, v2
	s_mov_b32 s81, s46
	v_writelane_b32 v253, s39, 57
	s_mov_b32 s83, s48
	s_barrier
	s_branch .LBB0_185

.LBB0_199:
	s_ashr_i32 s40, s36, 31
	s_lshr_b32 s40, s40, 26
	s_lshl_b32 s39, s39, 5
	s_add_i32 s40, s36, s40
	s_and_b32 s39, s39, 0x60
	s_ashr_i32 s74, s40, 6
	s_lshl_b32 s40, s37, 13
	s_lshl_b32 s41, s39, 7
	s_add_u32 s18, s18, 0x21400000
	s_addc_u32 s19, s19, 0
	v_lshl_add_u64 v[10:11], v[0:1], 0, s[56:57]
	s_add_i32 m0, s33, 0x18000
	s_nop 0
	global_load_lds_dwordx4 v[10:11], off
	v_lshl_add_u64 v[10:11], v[0:1], 0, s[0:1]
	s_add_i32 m0, s33, 0x1a000
	s_add_i32 s75, s33, 0x8000
	global_load_lds_dwordx4 v[10:11], off
	v_lshl_add_u64 v[10:11], v[2:3], 0, s[56:57]
	s_mov_b32 m0, s75
	s_add_i32 s77, s33, 0xa000
	global_load_lds_dwordx4 v[10:11], off
	v_lshl_add_u64 v[2:3], v[2:3], 0, s[0:1]
	s_mov_b32 m0, s77
	v_or_b32_e32 v134, s39, v9
	global_load_lds_dwordx4 v[2:3], off
	v_lshl_add_u64 v[2:3], v[0:1], 0, s[24:25]
	s_add_i32 m0, s33, 0x1c000
	v_lshl_add_u64 v[0:1], v[0:1], 0, s[26:27]
	global_load_lds_dwordx4 v[2:3], off
	s_add_i32 m0, s33, 0x1e000
	s_cmp_gt_i32 s36, 63
	global_load_lds_dwordx4 v[0:1], off
	s_waitcnt vmcnt(8)
	s_barrier
	v_and_b32_e32 v0, 15, v5
	v_lshlrev_b32_e32 v1, 1, v9
	v_lshl_or_b32 v132, s37, 6, v0
	v_lshl_or_b32 v0, v0, 6, v1
	v_lshlrev_b32_e32 v1, 2, v5
	s_cselect_b64 s[36:37], -1, 0
	s_add_i32 s78, s74, -2
	v_and_b32_e32 v1, 32, v1
	s_cmpk_lt_u32 s38, 0x100
	s_mov_b32 s38, s44
	v_bitop3_b32 v2, v0, s40, v1 bitop3:0xde
	v_bitop3_b32 v133, v0, s41, v1 bitop3:0xde
	v_lshlrev_b32_e32 v0, 8, v4
	v_writelane_b32 v253, s38, 52
	s_waitcnt vmcnt(6)
	v_and_b32_e32 v0, 0x18000, v0
	v_lshlrev_b32_e32 v1, 11, v6
	v_writelane_b32 v253, s39, 53
	s_mov_b32 s38, s42
	v_or3_b32 v0, v7, v0, v1
	v_writelane_b32 v253, s38, 50
	s_cselect_b64 s[40:41], -1, 0
	v_add_u32_e32 v130, v0, v8
	v_mov_b32_e32 v131, v161
	s_mov_b32 s96, 0
	v_add_u32_e32 v135, 0, v2
	s_mov_b32 s79, s44
	v_writelane_b32 v253, s39, 51
	s_mov_b32 s80, s42
	s_barrier
	s_branch .LBB0_202

.LBB0_332:
	s_add_u32 s36, s36, 0x13400000
	s_addc_u32 s37, s37, 0
	v_lshl_add_u64 v[10:11], v[0:1], 0, s[56:57]
	s_add_i32 m0, s59, 0x18000
	s_nop 0
	global_load_lds_dwordx4 v[10:11], off
	v_lshl_add_u64 v[10:11], v[0:1], 0, s[4:5]
	s_add_i32 m0, s59, 0x1a000
	s_add_i32 s79, s59, 0x8000
	global_load_lds_dwordx4 v[10:11], off
	v_lshl_add_u64 v[10:11], v[2:3], 0, s[56:57]
	s_mov_b32 m0, s79
	s_add_i32 s80, s59, 0xa000
	global_load_lds_dwordx4 v[10:11], off
	v_lshl_add_u64 v[2:3], v[2:3], 0, s[28:29]
	s_mov_b32 m0, s80
	s_ashr_i32 s34, s39, 31
	global_load_lds_dwordx4 v[2:3], off
	v_lshl_add_u64 v[2:3], v[0:1], 0, s[28:29]
	s_add_i32 m0, s59, 0x1c000
	v_lshl_add_u64 v[0:1], v[0:1], 0, s[12:13]
	global_load_lds_dwordx4 v[2:3], off
	s_add_i32 m0, s59, 0x1e000
	s_lshr_b32 s34, s34, 26
	global_load_lds_dwordx4 v[0:1], off
	s_waitcnt vmcnt(8)
	s_barrier
	v_and_b32_e32 v0, 15, v5
	v_lshlrev_b32_e32 v1, 1, v9
	s_add_i32 s34, s39, s34
	v_lshl_or_b32 v132, s41, 6, v0
	v_lshl_or_b32 v0, v0, 6, v1
	v_lshlrev_b32_e32 v1, 2, v5
	s_ashr_i32 s81, s34, 6
	s_lshl_b32 s34, s41, 13
	v_and_b32_e32 v1, 32, v1
	v_bitop3_b32 v2, v0, s34, v1 bitop3:0xde
	s_lshl_b32 s34, s40, 5
	s_and_b32 s34, s34, 0x60
	s_lshl_b32 s35, s34, 7
	v_bitop3_b32 v133, v0, s35, v1 bitop3:0xde
	s_cmp_gt_i32 s39, 63
	v_lshlrev_b32_e32 v0, 7, v4
	s_waitcnt vmcnt(6)
	s_cselect_b64 s[42:43], -1, 0
	s_add_i32 s83, s81, -2
	v_or_b32_e32 v134, s34, v9
	v_and_b32_e32 v0, 0xc000, v0
	v_lshlrev_b32_e32 v1, 10, v6
	s_mov_b32 s34, s46
	s_cmpk_lt_u32 s38, 0x100
	v_or3_b32 v0, v7, v0, v1
	v_readlane_b32 s87, v253, 58
	v_writelane_b32 v253, s34, 59
	s_cselect_b64 s[44:45], -1, 0
	v_add_u32_e32 v130, v0, v8
	v_mov_b32_e32 v131, v161
	s_mov_b32 s96, 0
	v_add_u32_e32 v135, 0, v2
	v_writelane_b32 v253, s35, 60
	s_mov_b32 s92, s46
	s_barrier
	s_waitcnt vmcnt(0)
	s_branch .LBB0_335

.LBB0_767:
	s_lshl_b32 s96, s72, 12
	s_lshl_b64 s[40:41], s[96:97], 2
	s_add_u32 s36, s36, s40
	s_addc_u32 s37, s37, s41
	s_add_i32 s78, s54, 0x18000
	v_lshl_add_u64 v[10:11], v[0:1], 0, s[56:57]
	s_mov_b32 m0, s78
	s_add_i32 s79, s54, 0x1a000
	s_nop 0
	global_load_lds_dwordx4 v[10:11], off
	v_lshl_add_u64 v[10:11], v[0:1], 0, s[28:29]
	s_mov_b32 m0, s79
	s_add_i32 s80, s54, 0x8000
	global_load_lds_dwordx4 v[10:11], off
	v_lshl_add_u64 v[10:11], v[2:3], 0, s[56:57]
	s_mov_b32 m0, s80
	s_add_i32 s81, s54, 0xa000
	global_load_lds_dwordx4 v[10:11], off
	v_lshl_add_u64 v[2:3], v[2:3], 0, s[28:29]
	s_mov_b32 m0, s81
	s_add_i32 s83, s54, 0x1c000
	global_load_lds_dwordx4 v[2:3], off
	v_lshl_add_u64 v[2:3], v[0:1], 0, s[0:1]
	s_mov_b32 m0, s83
	s_add_i32 s86, s54, 0x1e000
	global_load_lds_dwordx4 v[2:3], off
	v_lshl_add_u64 v[0:1], v[0:1], 0, s[4:5]
	s_mov_b32 m0, s86
	s_ashr_i32 s40, s11, 31
	global_load_lds_dwordx4 v[0:1], off
	s_waitcnt vmcnt(8)
	s_barrier
	s_lshr_b32 s40, s40, 26
	s_add_i32 s40, s11, s40
	s_and_b32 s39, s39, 3
	s_ashr_i32 s87, s40, 6
	s_lshl_b32 s90, s38, 13
	s_cmp_gt_i32 s11, 63
	s_cselect_b64 s[40:41], -1, 0
	s_add_i32 s91, s87, -2
	s_cmpk_lt_u32 s10, 0x100
	s_cselect_b64 s[42:43], -1, 0
	s_lshl_b32 s10, s38, 15
	s_lshl_b32 s11, s39, 13
	s_or_b32 s10, s11, s10
	v_and_b32_e32 v0, 15, v8
	s_ashr_i32 s11, s10, 31
	v_bfe_u32 v1, v8, 4, 2
	v_lshlrev_b32_e32 v3, 6, v0
	v_lshlrev_b32_e32 v0, 3, v0
	s_add_u32 s10, s22, s10
	v_lshlrev_b32_e32 v2, 3, v1
	v_lshl_or_b32 v3, v1, 4, v3
	v_lshl_or_b32 v0, v1, 7, v0
	v_mov_b32_e32 v1, v161
	s_addc_u32 s11, s23, s11
	v_lshlrev_b32_e32 v8, 2, v8
	v_lshl_add_u64 v[0:1], s[10:11], 0, v[0:1]
	s_mov_b64 s[4:5], 0x13400000
	v_and_b32_e32 v8, 32, v8
	v_lshl_add_u64 v[164:165], v[0:1], 0, s[4:5]
	v_lshlrev_b32_e32 v0, 7, v4
	s_mov_b32 s10, s44
	s_waitcnt vmcnt(6)
	v_xad_u32 v173, v3, v8, 0
	v_and_b32_e32 v0, 0xc000, v0
	v_lshlrev_b32_e32 v1, 10, v5
	v_writelane_b32 v253, s10, 61
	v_lshl_or_b32 v172, s39, 5, v2
	v_lshl_add_u32 v2, s39, 12, v173
	v_or3_b32 v0, v6, v0, v1
	v_writelane_b32 v253, s11, 62
	s_mov_b32 s22, s46
	v_add_u32_e32 v174, 0x10000, v2
	v_add_u32_e32 v175, 0x14000, v2
	v_add_u32_e32 v176, 0x18000, v2
	v_add_u32_e32 v177, 0x1c000, v2
	v_add_u32_e32 v178, 0x10400, v2
	v_add_u32_e32 v179, 0x10800, v2
	v_add_u32_e32 v180, 0x10c00, v2
	v_add_u32_e32 v181, 0x14400, v2
	v_add_u32_e32 v182, 0x14800, v2
	v_add_u32_e32 v183, 0x14c00, v2
	v_add_u32_e32 v184, 0x18400, v2
	v_add_u32_e32 v185, 0x18800, v2
	v_add_u32_e32 v186, 0x18c00, v2
	v_add_u32_e32 v187, 0x1c400, v2
	v_add_u32_e32 v188, 0x1c800, v2
	v_add_u32_e32 v189, 0x1cc00, v2
	v_add_u32_e32 v166, v0, v7
	v_mov_b32_e32 v167, v161
	s_mov_b32 s96, 0
	s_mov_b32 s10, s44
	v_writelane_b32 v253, s22, 63
	s_mov_b32 s11, s46
	s_barrier
	v_writelane_b32 v254, s23, 0
	s_branch .LBB0_770

.LBB0_844:
	s_add_u32 s36, s18, 0x1b400000
	s_addc_u32 s37, s19, 0
	v_lshl_add_u64 v[8:9], v[0:1], 0, s[56:57]
	s_add_i32 m0, s59, 0x18000
	s_nop 0
	global_load_lds_dwordx4 v[8:9], off
	v_lshl_add_u64 v[8:9], v[0:1], 0, s[28:29]
	s_add_i32 m0, s59, 0x1a000
	s_add_i32 s79, s59, 0x8000
	global_load_lds_dwordx4 v[8:9], off
	v_lshl_add_u64 v[8:9], v[2:3], 0, s[56:57]
	s_mov_b32 m0, s79
	s_add_i32 s10, s59, 0xa000
	global_load_lds_dwordx4 v[8:9], off
	v_lshl_add_u64 v[2:3], v[2:3], 0, s[12:13]
	s_mov_b32 m0, s10
	s_and_b32 s41, s11, 3
	global_load_lds_dwordx4 v[2:3], off
	v_lshl_add_u64 v[2:3], v[0:1], 0, s[0:1]
	s_add_i32 m0, s59, 0x1c000
	v_lshl_add_u64 v[0:1], v[0:1], 0, s[4:5]
	global_load_lds_dwordx4 v[2:3], off
	s_add_i32 m0, s59, 0x1e000
	s_ashr_i32 s11, s39, 31
	global_load_lds_dwordx4 v[0:1], off
	s_waitcnt vmcnt(8)
	s_barrier
	v_bfe_u32 v1, v4, 4, 2
	v_and_b32_e32 v0, 15, v4
	s_lshr_b32 s11, s11, 26
	v_lshlrev_b32_e32 v3, 4, v1
	v_lshlrev_b32_e32 v4, 2, v4
	s_add_i32 s11, s39, s11
	v_lshl_or_b32 v3, v0, 6, v3
	s_lshl_b32 s42, s40, 13
	v_and_b32_e32 v4, 32, v4
	s_ashr_i32 s11, s11, 6
	v_bitop3_b32 v8, v3, s42, v4 bitop3:0xde
	s_lshl_b32 s42, s41, 12
	s_cmp_gt_i32 s39, 63
	s_cselect_b64 s[48:49], -1, 0
	s_add_i32 s80, s11, -2
	s_cmpk_lt_u32 s38, 0x100
	s_cselect_b64 s[50:51], -1, 0
	s_lshl_b32 s38, s40, 15
	s_lshl_b32 s39, s41, 13
	s_or_b32 s38, s39, s38
	s_ashr_i32 s39, s38, 31
	v_lshl_or_b32 v174, s40, 6, v0
	v_lshlrev_b32_e32 v0, 3, v0
	s_add_u32 s18, s18, s38
	v_lshl_or_b32 v160, v1, 7, v0
	s_addc_u32 s19, s19, s39
	v_lshlrev_b32_e32 v2, 3, v1
	s_waitcnt vmcnt(6)
	v_lshl_add_u64 v[0:1], s[18:19], 0, v[160:161]
	s_mov_b64 s[4:5], 0x13400000
	v_mov_b32_e32 v160, v161
	v_bitop3_b32 v175, v3, s42, v4 bitop3:0xde
	v_lshl_or_b32 v176, s41, 5, v2
	v_lshl_add_u64 v[132:133], v[0:1], 0, s[4:5]
	v_add3_u32 v134, v7, v5, v6
	v_mov_b32_e32 v162, v161
	v_mov_b32_e32 v163, v161
	v_add_u32_e32 v177, 0, v8
	v_mov_b64_e32 v[0:1], v[160:161]
	v_mov_b64_e32 v[4:5], v[160:161]
	v_mov_b64_e32 v[8:9], v[160:161]
	v_mov_b64_e32 v[12:13], v[160:161]
	v_mov_b64_e32 v[16:17], v[160:161]
	v_mov_b64_e32 v[20:21], v[160:161]
	v_mov_b64_e32 v[24:25], v[160:161]
	v_mov_b64_e32 v[28:29], v[160:161]
	v_mov_b64_e32 v[32:33], v[160:161]
	v_mov_b64_e32 v[36:37], v[160:161]
	v_mov_b64_e32 v[40:41], v[160:161]
	v_mov_b64_e32 v[44:45], v[160:161]
	v_mov_b64_e32 v[48:49], v[160:161]
	v_mov_b64_e32 v[52:53], v[160:161]
	v_mov_b64_e32 v[56:57], v[160:161]
	v_mov_b64_e32 v[60:61], v[160:161]
	v_mov_b64_e32 v[64:65], v[160:161]
	v_mov_b64_e32 v[68:69], v[160:161]
	v_mov_b64_e32 v[72:73], v[160:161]
	v_mov_b64_e32 v[76:77], v[160:161]
	v_mov_b64_e32 v[80:81], v[160:161]
	v_mov_b64_e32 v[84:85], v[160:161]
	v_mov_b64_e32 v[88:89], v[160:161]
	v_mov_b64_e32 v[92:93], v[160:161]
	v_mov_b64_e32 v[96:97], v[160:161]
	v_mov_b64_e32 v[100:101], v[160:161]
	v_mov_b64_e32 v[104:105], v[160:161]
	v_mov_b64_e32 v[108:109], v[160:161]
	v_mov_b64_e32 v[112:113], v[160:161]
	v_mov_b64_e32 v[116:117], v[160:161]
	v_mov_b64_e32 v[120:121], v[160:161]
	v_mov_b64_e32 v[124:125], v[160:161]
	v_mov_b32_e32 v135, v161
	s_mov_b32 s38, 0
	v_mov_b64_e32 v[2:3], v[162:163]
	v_mov_b64_e32 v[6:7], v[162:163]
	v_mov_b64_e32 v[10:11], v[162:163]
	v_mov_b64_e32 v[14:15], v[162:163]
	v_mov_b64_e32 v[18:19], v[162:163]
	v_mov_b64_e32 v[22:23], v[162:163]
	v_mov_b64_e32 v[26:27], v[162:163]
	v_mov_b64_e32 v[30:31], v[162:163]
	v_mov_b64_e32 v[34:35], v[162:163]
	v_mov_b64_e32 v[38:39], v[162:163]
	v_mov_b64_e32 v[42:43], v[162:163]
	v_mov_b64_e32 v[46:47], v[162:163]
	v_mov_b64_e32 v[50:51], v[162:163]
	v_mov_b64_e32 v[54:55], v[162:163]
	v_mov_b64_e32 v[58:59], v[162:163]
	v_mov_b64_e32 v[62:63], v[162:163]
	v_mov_b64_e32 v[66:67], v[162:163]
	v_mov_b64_e32 v[70:71], v[162:163]
	v_mov_b64_e32 v[74:75], v[162:163]
	v_mov_b64_e32 v[78:79], v[162:163]
	v_mov_b64_e32 v[82:83], v[162:163]
	v_mov_b64_e32 v[86:87], v[162:163]
	v_mov_b64_e32 v[90:91], v[162:163]
	v_mov_b64_e32 v[94:95], v[162:163]
	v_mov_b64_e32 v[98:99], v[162:163]
	v_mov_b64_e32 v[102:103], v[162:163]
	v_mov_b64_e32 v[106:107], v[162:163]
	v_mov_b64_e32 v[110:111], v[162:163]
	v_mov_b64_e32 v[114:115], v[162:163]
	v_mov_b64_e32 v[118:119], v[162:163]
	v_mov_b64_e32 v[122:123], v[162:163]
	v_mov_b64_e32 v[126:127], v[162:163]
	s_mov_b32 s81, 0
	s_barrier
	s_branch .LBB0_847

.LBB0_1060:
	s_add_u32 s42, s34, 0x2400000
	s_addc_u32 s43, s35, 0
	v_lshl_add_u64 v[10:11], v[0:1], 0, s[56:57]
	s_add_i32 m0, s7, 0x18000
	s_nop 0
	global_load_lds_dwordx4 v[10:11], off
	v_lshl_add_u64 v[10:11], v[0:1], 0, s[0:1]
	s_add_i32 m0, s7, 0x1a000
	s_add_i32 s77, s7, 0x8000
	global_load_lds_dwordx4 v[10:11], off
	v_lshl_add_u64 v[10:11], v[2:3], 0, s[56:57]
	s_mov_b32 m0, s77
	s_add_i32 s78, s7, 0xa000
	global_load_lds_dwordx4 v[10:11], off
	v_lshl_add_u64 v[2:3], v[2:3], 0, s[0:1]
	s_mov_b32 m0, s78
	s_ashr_i32 s40, s19, 31
	global_load_lds_dwordx4 v[2:3], off
	v_lshl_add_u64 v[2:3], v[0:1], 0, s[24:25]
	s_add_i32 m0, s7, 0x1c000
	v_lshl_add_u64 v[0:1], v[0:1], 0, s[26:27]
	global_load_lds_dwordx4 v[2:3], off
	s_add_i32 m0, s7, 0x1e000
	s_lshr_b32 s40, s40, 26
	global_load_lds_dwordx4 v[0:1], off
	s_waitcnt vmcnt(8)
	s_barrier
	v_bfe_u32 v1, v7, 4, 2
	v_and_b32_e32 v0, 15, v7
	v_lshlrev_b32_e32 v2, 4, v1
	v_lshl_or_b32 v152, s39, 6, v0
	v_lshl_or_b32 v0, v0, 6, v2
	v_lshlrev_b32_e32 v2, 2, v7
	s_lshl_b32 s38, s38, 5
	s_add_i32 s40, s19, s40
	s_lshl_b32 s39, s39, 13
	v_and_b32_e32 v2, 32, v2
	s_and_b32 s38, s38, 0x60
	s_ashr_i32 s79, s40, 6
	v_bitop3_b32 v3, v0, s39, v2 bitop3:0xde
	s_lshl_b32 s39, s38, 7
	s_cmp_gt_i32 s19, 63
	s_cselect_b64 s[44:45], -1, 0
	s_add_i32 s80, s79, -2
	v_bitop3_b32 v153, v0, s39, v2 bitop3:0xde
	s_cmpk_lt_u32 s18, 0x100
	v_lshlrev_b32_e32 v0, 8, v4
	v_readlane_b32 s18, v254, 1
	s_waitcnt vmcnt(6)
	v_lshl_or_b32 v154, v1, 2, s38
	v_and_b32_e32 v0, 0x18000, v0
	v_lshlrev_b32_e32 v1, 11, v8
	v_readlane_b32 s19, v254, 2
	v_or3_b32 v0, v6, v0, v1
	s_mov_b32 s81, s18
	v_readlane_b32 s18, v254, 3
	s_cselect_b64 s[46:47], -1, 0
	v_add_u32_e32 v128, v0, v5
	v_mov_b32_e32 v129, v161
	s_mov_b32 s96, 0
	v_add_u32_e32 v155, 0, v3
	s_mov_b32 s83, s18
	s_barrier
	v_readlane_b32 s19, v254, 4
	s_branch .LBB0_1063

.LBB0_1083:
	s_add_u32 s34, s34, 0x2400000
	s_addc_u32 s35, s35, 0
	v_lshl_add_u64 v[10:11], v[0:1], 0, s[56:57]
	s_add_i32 m0, s7, 0x18000
	s_nop 0
	global_load_lds_dwordx4 v[10:11], off
	v_lshl_add_u64 v[10:11], v[0:1], 0, s[0:1]
	s_add_i32 m0, s7, 0x1a000
	s_add_i32 s77, s7, 0x8000
	global_load_lds_dwordx4 v[10:11], off
	v_lshl_add_u64 v[10:11], v[2:3], 0, s[56:57]
	s_mov_b32 m0, s77
	s_add_i32 s78, s7, 0xa000
	global_load_lds_dwordx4 v[10:11], off
	v_lshl_add_u64 v[2:3], v[2:3], 0, s[0:1]
	s_mov_b32 m0, s78
	s_ashr_i32 s42, s39, 31
	global_load_lds_dwordx4 v[2:3], off
	v_lshl_add_u64 v[2:3], v[0:1], 0, s[24:25]
	s_add_i32 m0, s7, 0x1c000
	v_lshl_add_u64 v[0:1], v[0:1], 0, s[26:27]
	global_load_lds_dwordx4 v[2:3], off
	s_add_i32 m0, s7, 0x1e000
	s_lshr_b32 s42, s42, 26
	global_load_lds_dwordx4 v[0:1], off
	s_waitcnt vmcnt(8)
	s_barrier
	v_bfe_u32 v1, v7, 4, 2
	v_and_b32_e32 v0, 15, v7
	v_lshlrev_b32_e32 v2, 4, v1
	v_lshl_or_b32 v134, s41, 6, v0
	v_lshl_or_b32 v0, v0, 6, v2
	v_lshlrev_b32_e32 v2, 2, v7
	s_lshl_b32 s40, s40, 5
	s_add_i32 s42, s39, s42
	s_lshl_b32 s41, s41, 13
	v_and_b32_e32 v2, 32, v2
	s_and_b32 s40, s40, 0x60
	s_ashr_i32 s79, s42, 6
	v_bitop3_b32 v3, v0, s41, v2 bitop3:0xde
	s_lshl_b32 s41, s40, 7
	s_cmp_gt_i32 s39, 63
	s_cselect_b64 s[42:43], -1, 0
	s_add_i32 s80, s79, -2
	v_bitop3_b32 v135, v0, s41, v2 bitop3:0xde
	s_cmpk_lt_u32 s38, 0x100
	v_lshlrev_b32_e32 v0, 8, v4
	v_readlane_b32 s38, v254, 1
	s_waitcnt vmcnt(6)
	v_lshl_or_b32 v136, v1, 2, s40
	v_and_b32_e32 v0, 0x18000, v0
	v_lshlrev_b32_e32 v1, 11, v8
	v_readlane_b32 s39, v254, 2
	v_or3_b32 v0, v6, v0, v1
	s_mov_b32 s81, s38
	v_readlane_b32 s38, v254, 3
	s_cselect_b64 s[44:45], -1, 0
	v_add_u32_e32 v128, v0, v5
	v_mov_b32_e32 v129, v161
	s_mov_b32 s96, 0
	v_add_u32_e32 v137, 0, v3
	s_mov_b32 s83, s38
	s_barrier
	v_readlane_b32 s39, v254, 4
	s_branch .LBB0_1086

.LBB0_1225:
	s_add_u32 s34, s34, 0x10c00000
	s_addc_u32 s35, s35, 0
	v_lshl_add_u64 v[10:11], v[0:1], 0, s[56:57]
	s_add_i32 m0, s33, 0x18000
	s_nop 0
	global_load_lds_dwordx4 v[10:11], off
	v_lshl_add_u64 v[10:11], v[0:1], 0, s[0:1]
	s_add_i32 m0, s33, 0x1a000
	s_add_i32 s74, s33, 0x8000
	global_load_lds_dwordx4 v[10:11], off
	v_lshl_add_u64 v[10:11], v[2:3], 0, s[56:57]
	s_mov_b32 m0, s74
	s_add_i32 s75, s33, 0xa000
	global_load_lds_dwordx4 v[10:11], off
	v_lshl_add_u64 v[2:3], v[2:3], 0, s[0:1]
	s_mov_b32 m0, s75
	s_ashr_i32 s40, s37, 31
	global_load_lds_dwordx4 v[2:3], off
	v_lshl_add_u64 v[2:3], v[0:1], 0, s[24:25]
	s_add_i32 m0, s33, 0x1c000
	v_lshl_add_u64 v[0:1], v[0:1], 0, s[26:27]
	global_load_lds_dwordx4 v[2:3], off
	s_add_i32 m0, s33, 0x1e000
	s_lshr_b32 s40, s40, 26
	global_load_lds_dwordx4 v[0:1], off
	s_waitcnt vmcnt(8)
	s_barrier
	v_and_b32_e32 v0, 15, v5
	v_lshlrev_b32_e32 v1, 1, v9
	v_lshl_or_b32 v134, s39, 6, v0
	v_lshl_or_b32 v0, v0, 6, v1
	v_lshlrev_b32_e32 v1, 2, v5
	s_lshl_b32 s38, s38, 5
	s_add_i32 s40, s37, s40
	s_lshl_b32 s39, s39, 13
	v_and_b32_e32 v1, 32, v1
	s_and_b32 s38, s38, 0x60
	s_ashr_i32 s77, s40, 6
	v_bitop3_b32 v2, v0, s39, v1 bitop3:0xde
	s_lshl_b32 s39, s38, 7
	s_cmp_gt_i32 s37, 63
	s_cselect_b64 s[40:41], -1, 0
	s_add_i32 s78, s77, -2
	s_cmpk_lt_u32 s36, 0x100
	s_mov_b32 s36, s44
	v_bitop3_b32 v135, v0, s39, v1 bitop3:0xde
	v_lshlrev_b32_e32 v0, 8, v4
	v_writelane_b32 v254, s36, 5
	s_waitcnt vmcnt(6)
	v_and_b32_e32 v0, 0x18000, v0
	v_lshlrev_b32_e32 v1, 11, v6
	v_writelane_b32 v254, s37, 6
	s_mov_b32 s36, s46
	v_or3_b32 v0, v7, v0, v1
	v_writelane_b32 v254, s36, 10
	s_cselect_b64 s[42:43], -1, 0
	v_or_b32_e32 v136, s38, v9
	v_add_u32_e32 v130, v0, v8
	v_mov_b32_e32 v131, v161
	s_mov_b32 s96, 0
	v_add_u32_e32 v137, 0, v2
	s_mov_b32 s79, s44
	v_writelane_b32 v254, s37, 11
	s_mov_b32 s80, s46
	s_barrier
	s_branch .LBB0_1228

.LBB0_1296:
	s_add_u32 s40, s18, 0x2400000
	s_addc_u32 s41, s19, 0
	v_lshl_add_u64 v[8:9], v[0:1], 0, s[56:57]
	s_add_i32 m0, s33, 0x18000
	s_nop 0
	global_load_lds_dwordx4 v[8:9], off
	v_lshl_add_u64 v[8:9], v[0:1], 0, s[4:5]
	s_add_i32 m0, s33, 0x1a000
	s_add_i32 s51, s33, 0x8000
	global_load_lds_dwordx4 v[8:9], off
	v_lshl_add_u64 v[8:9], v[2:3], 0, s[56:57]
	s_mov_b32 m0, s51
	s_add_i32 s54, s33, 0xa000
	global_load_lds_dwordx4 v[8:9], off
	v_lshl_add_u64 v[2:3], v[2:3], 0, s[4:5]
	s_mov_b32 m0, s54
	s_ashr_i32 s18, s37, 31
	global_load_lds_dwordx4 v[2:3], off
	v_lshl_add_u64 v[2:3], v[0:1], 0, s[12:13]
	s_add_i32 m0, s33, 0x1c000
	v_lshl_add_u64 v[0:1], v[0:1], 0, s[42:43]
	global_load_lds_dwordx4 v[2:3], off
	s_add_i32 m0, s33, 0x1e000
	s_lshr_b32 s18, s18, 26
	global_load_lds_dwordx4 v[0:1], off
	s_waitcnt vmcnt(8)
	s_barrier
	v_bfe_u32 v1, v4, 4, 2
	v_and_b32_e32 v0, 15, v4
	v_lshlrev_b32_e32 v2, 4, v1
	s_add_i32 s18, s37, s18
	v_lshl_or_b32 v152, s39, 6, v0
	v_lshl_or_b32 v0, v0, 6, v2
	v_lshlrev_b32_e32 v2, 2, v4
	s_ashr_i32 s55, s18, 6
	s_lshl_b32 s18, s39, 13
	v_and_b32_e32 v2, 32, v2
	v_bitop3_b32 v3, v0, s18, v2 bitop3:0xde
	s_lshl_b32 s18, s38, 5
	s_and_b32 s18, s18, 0x60
	s_lshl_b32 s19, s18, 7
	v_bitop3_b32 v153, v0, s19, v2 bitop3:0xde
	s_cmp_gt_i32 s37, 63
	v_lshl_or_b32 v154, v1, 2, s18
	v_readlane_b32 s18, v254, 1
	s_waitcnt vmcnt(6)
	s_cselect_b64 s[42:43], -1, 0
	s_add_i32 s58, s55, -2
	v_readlane_b32 s19, v254, 2
	s_cmpk_lt_u32 s36, 0x100
	s_mov_b32 s74, s18
	v_readlane_b32 s18, v254, 3
	s_cselect_b64 s[44:45], -1, 0
	v_add3_u32 v128, v7, v6, v5
	v_mov_b32_e32 v129, v161
	s_mov_b32 s96, 0
	v_add_u32_e32 v155, 0, v3
	s_mov_b32 s75, s18
	s_barrier
	v_readlane_b32 s19, v254, 4
	s_branch .LBB0_1299

.LBB0_1523:
	s_add_u32 s40, s36, 0xfa00000
	s_addc_u32 s41, s37, 0
	s_add_i32 s91, s75, 0x18000
	v_lshl_add_u64 v[10:11], v[0:1], 0, s[56:57]
	s_mov_b32 m0, s91
	s_add_i32 s92, s75, 0x1a000
	s_nop 0
	global_load_lds_dwordx4 v[10:11], off
	v_lshl_add_u64 v[10:11], v[0:1], 0, s[28:29]
	s_mov_b32 m0, s92
	s_add_i32 s93, s75, 0x8000
	global_load_lds_dwordx4 v[10:11], off
	v_lshl_add_u64 v[10:11], v[2:3], 0, s[56:57]
	s_mov_b32 m0, s93
	s_add_i32 s95, s75, 0xa000
	global_load_lds_dwordx4 v[10:11], off
	v_lshl_add_u64 v[2:3], v[2:3], 0, s[28:29]
	s_mov_b32 m0, s95
	s_add_i32 s11, s75, 0x1c000
	global_load_lds_dwordx4 v[2:3], off
	v_lshl_add_u64 v[2:3], v[0:1], 0, s[0:1]
	s_mov_b32 m0, s11
	s_mov_b64 s[4:5], 0x30080
	s_add_i32 s31, s75, 0x1e000
	global_load_lds_dwordx4 v[2:3], off
	v_lshl_add_u64 v[0:1], v[0:1], 0, s[4:5]
	s_mov_b32 m0, s31
	s_ashr_i32 s10, s6, 31
	global_load_lds_dwordx4 v[0:1], off
	s_waitcnt vmcnt(8)
	s_barrier
	s_lshr_b32 s10, s10, 26
	s_lshl_b32 s35, s35, 5
	v_and_b32_e32 v0, 15, v5
	s_add_i32 s10, s6, s10
	s_and_b32 s35, s35, 0x60
	s_ashr_i32 s10, s10, 6
	v_lshl_or_b32 v170, s34, 6, v0
	s_lshl_b32 s34, s34, 13
	v_lshlrev_b32_e32 v2, 2, v5
	s_lshl_b32 s36, s35, 7
	v_lshlrev_b32_e32 v1, 1, v9
	v_lshlrev_b32_e32 v0, 6, v0
	v_and_b32_e32 v2, 32, v2
	s_cmp_gt_i32 s6, 63
	v_bitop3_b32 v0, v0, v2, v1 bitop3:0x36
	s_cselect_b64 s[42:43], -1, 0
	s_add_i32 s36, s36, 0
	v_add_u32_e32 v1, s36, v0
	v_add_u32_e32 v171, 0x10000, v1
	v_add_u32_e32 v172, 0x14000, v1
	v_add_u32_e32 v173, 0x18000, v1
	v_add_u32_e32 v174, 0x1c000, v1
	v_add_u32_e32 v175, 0x10400, v1
	v_add_u32_e32 v176, 0x10800, v1
	v_add_u32_e32 v177, 0x10c00, v1
	v_add_u32_e32 v178, 0x14400, v1
	v_add_u32_e32 v179, 0x14800, v1
	v_add_u32_e32 v180, 0x14c00, v1
	v_add_u32_e32 v181, 0x18400, v1
	v_add_u32_e32 v182, 0x18800, v1
	v_add_u32_e32 v183, 0x18c00, v1
	v_add_u32_e32 v184, 0x1c400, v1
	v_add_u32_e32 v185, 0x1c800, v1
	v_add_u32_e32 v186, 0x1cc00, v1
	v_lshlrev_b32_e32 v1, 7, v4
	s_waitcnt vmcnt(6)
	s_add_i32 s6, s10, -2
	v_and_b32_e32 v1, 0xc000, v1
	v_lshlrev_b32_e32 v2, 10, v6
	v_add_u32_e32 v0, 0, v0
	s_cmpk_lt_u32 s19, 0x100
	v_or3_b32 v1, v7, v1, v2
	s_cselect_b64 s[44:45], -1, 0
	s_mov_b32 s19, s97
	v_or_b32_e32 v187, s35, v9
	v_add_u32_e32 v164, v1, v8
	v_mov_b32_e32 v165, v161
	s_mov_b32 s96, 0
	v_add_u32_e32 v188, s34, v0
	s_barrier
	s_branch .LBB0_1526

.LBB0_1604:
	s_add_u32 s40, s36, 0x1da00000
	s_addc_u32 s41, s37, 0
	s_add_i32 s79, s55, 0x18000
	v_lshl_add_u64 v[10:11], v[0:1], 0, s[56:57]
	s_mov_b32 m0, s79
	s_mov_b64 s[4:5], 0x38080
	s_add_i32 s80, s55, 0x1a000
	s_nop 0
	global_load_lds_dwordx4 v[10:11], off
	v_lshl_add_u64 v[10:11], v[0:1], 0, s[4:5]
	s_mov_b32 m0, s80
	s_add_i32 s81, s55, 0x8000
	global_load_lds_dwordx4 v[10:11], off
	v_lshl_add_u64 v[10:11], v[2:3], 0, s[56:57]
	s_mov_b32 m0, s81
	s_add_i32 s83, s55, 0xa000
	global_load_lds_dwordx4 v[10:11], off
	v_lshl_add_u64 v[2:3], v[2:3], 0, s[4:5]
	s_mov_b32 m0, s83
	s_mov_b64 s[4:5], 0x70080
	s_add_i32 s86, s55, 0x1c000
	global_load_lds_dwordx4 v[2:3], off
	v_lshl_add_u64 v[2:3], v[0:1], 0, s[4:5]
	s_mov_b32 m0, s86
	s_mov_b64 s[4:5], 0xa8080
	s_add_i32 s87, s55, 0x1e000
	global_load_lds_dwordx4 v[2:3], off
	v_lshl_add_u64 v[0:1], v[0:1], 0, s[4:5]
	s_mov_b32 m0, s87
	s_ashr_i32 s36, s11, 31
	global_load_lds_dwordx4 v[0:1], off
	s_waitcnt vmcnt(8)
	s_barrier
	s_lshr_b32 s36, s36, 26
	v_and_b32_e32 v0, 15, v4
	s_add_i32 s36, s11, s36
	s_ashr_i32 s90, s36, 6
	v_lshl_or_b32 v170, s19, 6, v0
	s_lshl_b32 s36, s19, 13
	s_lshl_b32 s19, s38, 5
	s_and_b32 s37, s19, 0x60
	v_lshlrev_b32_e32 v2, 2, v4
	s_lshl_b32 s19, s37, 7
	v_lshlrev_b32_e32 v1, 1, v7
	v_lshlrev_b32_e32 v0, 6, v0
	v_and_b32_e32 v2, 32, v2
	s_cmp_gt_i32 s11, 63
	v_bitop3_b32 v0, v0, v2, v1 bitop3:0x36
	s_cselect_b64 s[42:43], -1, 0
	s_add_i32 s19, s19, 0
	v_add_u32_e32 v1, s19, v0
	s_waitcnt vmcnt(6)
	s_add_i32 s91, s90, -2
	v_add_u32_e32 v171, 0x10000, v1
	v_add_u32_e32 v172, 0x14000, v1
	v_add_u32_e32 v173, 0x18000, v1
	v_add_u32_e32 v174, 0x1c000, v1
	v_add_u32_e32 v175, 0x10400, v1
	v_add_u32_e32 v176, 0x10800, v1
	v_add_u32_e32 v177, 0x10c00, v1
	v_add_u32_e32 v178, 0x14400, v1
	v_add_u32_e32 v179, 0x14800, v1
	v_add_u32_e32 v180, 0x14c00, v1
	v_add_u32_e32 v181, 0x18400, v1
	v_add_u32_e32 v182, 0x18800, v1
	v_add_u32_e32 v183, 0x18c00, v1
	v_add_u32_e32 v184, 0x1c400, v1
	v_add_u32_e32 v185, 0x1c800, v1
	v_add_u32_e32 v186, 0x1cc00, v1
	v_add_u16_e32 v1, v5, v6
	v_add_u32_e32 v0, 0, v0
	s_cmpk_lt_u32 s6, 0x100
	v_lshrrev_b16_e32 v1, 1, v1
	s_cselect_b64 s[44:45], -1, 0
	s_mov_b32 s19, s97
	v_or_b32_e32 v187, s37, v7
	v_add_lshl_u32 v164, v8, v1, 1
	v_mov_b32_e32 v165, v161
	s_mov_b32 s96, 0
	v_add_u32_e32 v188, s36, v0
	s_barrier
	s_branch .LBB0_1607

.LBB0_1692:
	s_add_u32 s42, s36, 0xfa00000
	s_addc_u32 s43, s37, 0
	s_add_i32 s91, s77, 0x18000
	v_lshl_add_u64 v[10:11], v[0:1], 0, s[56:57]
	s_mov_b32 m0, s91
	s_add_i32 s93, s77, 0x1a000
	s_nop 0
	global_load_lds_dwordx4 v[10:11], off
	v_lshl_add_u64 v[10:11], v[0:1], 0, s[28:29]
	s_mov_b32 m0, s93
	s_add_i32 s95, s77, 0x8000
	global_load_lds_dwordx4 v[10:11], off
	v_lshl_add_u64 v[10:11], v[2:3], 0, s[56:57]
	s_mov_b32 m0, s95
	s_add_i32 s40, s77, 0xa000
	global_load_lds_dwordx4 v[10:11], off
	v_lshl_add_u64 v[2:3], v[2:3], 0, s[28:29]
	s_mov_b32 m0, s40
	s_add_i32 s41, s77, 0x1c000
	global_load_lds_dwordx4 v[2:3], off
	v_lshl_add_u64 v[2:3], v[0:1], 0, s[0:1]
	s_mov_b32 m0, s41
	s_mov_b64 s[4:5], 0x30080
	s_add_i32 s31, s77, 0x1e000
	global_load_lds_dwordx4 v[2:3], off
	v_lshl_add_u64 v[0:1], v[0:1], 0, s[4:5]
	s_mov_b32 m0, s31
	s_ashr_i32 s11, s7, 31
	global_load_lds_dwordx4 v[0:1], off
	s_waitcnt vmcnt(8)
	s_barrier
	s_lshr_b32 s11, s11, 26
	s_lshl_b32 s35, s35, 5
	v_and_b32_e32 v0, 15, v5
	s_add_i32 s11, s7, s11
	s_and_b32 s36, s35, 0x60
	s_ashr_i32 s11, s11, 6
	v_lshl_or_b32 v170, s19, 6, v0
	s_lshl_b32 s19, s19, 13
	v_lshlrev_b32_e32 v2, 2, v5
	s_lshl_b32 s35, s36, 7
	v_lshlrev_b32_e32 v1, 1, v9
	v_lshlrev_b32_e32 v0, 6, v0
	v_and_b32_e32 v2, 32, v2
	s_cmp_gt_i32 s7, 63
	v_bitop3_b32 v0, v0, v2, v1 bitop3:0x36
	s_cselect_b64 s[44:45], -1, 0
	s_add_i32 s35, s35, 0
	v_add_u32_e32 v1, s35, v0
	v_add_u32_e32 v171, 0x10000, v1
	v_add_u32_e32 v172, 0x14000, v1
	v_add_u32_e32 v173, 0x18000, v1
	v_add_u32_e32 v174, 0x1c000, v1
	v_add_u32_e32 v175, 0x10400, v1
	v_add_u32_e32 v176, 0x10800, v1
	v_add_u32_e32 v177, 0x10c00, v1
	v_add_u32_e32 v178, 0x14400, v1
	v_add_u32_e32 v179, 0x14800, v1
	v_add_u32_e32 v180, 0x14c00, v1
	v_add_u32_e32 v181, 0x18400, v1
	v_add_u32_e32 v182, 0x18800, v1
	v_add_u32_e32 v183, 0x18c00, v1
	v_add_u32_e32 v184, 0x1c400, v1
	v_add_u32_e32 v185, 0x1c800, v1
	v_add_u32_e32 v186, 0x1cc00, v1
	v_lshlrev_b32_e32 v1, 7, v4
	s_waitcnt vmcnt(6)
	s_add_i32 s7, s11, -2
	v_and_b32_e32 v1, 0xc000, v1
	v_lshlrev_b32_e32 v2, 10, v6
	v_add_u32_e32 v0, 0, v0
	s_cmpk_lt_u32 s18, 0x100
	v_or3_b32 v1, v7, v1, v2
	s_cselect_b64 s[46:47], -1, 0
	s_mov_b32 s35, s97
	v_or_b32_e32 v187, s36, v9
	v_add_u32_e32 v164, v1, v8
	v_mov_b32_e32 v165, v161
	s_mov_b32 s96, 0
	v_add_u32_e32 v188, s19, v0
	s_barrier
	s_branch .LBB0_1695

.LBB0_1769:
	s_add_u32 s40, s36, 0xb800000
	s_addc_u32 s41, s37, 0
	s_add_i32 s75, s31, 0x18000
	v_lshl_add_u64 v[8:9], v[0:1], 0, s[56:57]
	s_mov_b32 m0, s75
	s_add_i32 s77, s31, 0x1a000
	s_nop 0
	global_load_lds_dwordx4 v[8:9], off
	v_lshl_add_u64 v[8:9], v[0:1], 0, s[12:13]
	s_mov_b32 m0, s77
	s_add_i32 s78, s31, 0x8000
	global_load_lds_dwordx4 v[8:9], off
	v_lshl_add_u64 v[8:9], v[2:3], 0, s[56:57]
	s_mov_b32 m0, s78
	s_add_i32 s79, s31, 0xa000
	global_load_lds_dwordx4 v[8:9], off
	v_lshl_add_u64 v[2:3], v[2:3], 0, s[12:13]
	s_mov_b32 m0, s79
	s_add_i32 s80, s31, 0x1c000
	global_load_lds_dwordx4 v[2:3], off
	v_lshl_add_u64 v[2:3], v[0:1], 0, s[4:5]
	s_mov_b32 m0, s80
	s_add_i32 s81, s31, 0x1e000
	global_load_lds_dwordx4 v[2:3], off
	v_lshl_add_u64 v[0:1], v[0:1], 0, s[46:47]
	s_mov_b32 m0, s81
	s_ashr_i32 s36, s42, 31
	global_load_lds_dwordx4 v[0:1], off
	s_waitcnt vmcnt(8)
	s_barrier
	s_lshr_b32 s36, s36, 26
	s_lshl_b32 s37, s43, 5
	v_and_b32_e32 v0, 15, v7
	s_add_i32 s36, s42, s36
	s_and_b32 s37, s37, 0x60
	v_bfe_u32 v1, v7, 4, 2
	s_ashr_i32 s83, s36, 6
	v_lshl_or_b32 v168, s45, 6, v0
	s_lshl_b32 s36, s45, 13
	v_lshlrev_b32_e32 v3, 2, v7
	s_lshl_b32 s45, s37, 7
	v_lshlrev_b32_e32 v2, 4, v1
	v_lshlrev_b32_e32 v0, 6, v0
	v_and_b32_e32 v3, 32, v3
	s_cmp_gt_i32 s42, 63
	v_bitop3_b32 v0, v0, v3, v2 bitop3:0x36
	s_cselect_b64 s[42:43], -1, 0
	s_add_i32 s45, s45, 0
	s_waitcnt vmcnt(6)
	s_add_i32 s86, s83, -2
	v_add_u32_e32 v2, s45, v0
	v_add_u32_e32 v0, 0, v0
	s_cmpk_lt_u32 s44, 0x100
	v_lshl_or_b32 v185, v1, 2, s37
	v_add_u32_e32 v186, s36, v0
	v_readlane_b32 s36, v253, 45
	v_add_u32_e32 v169, 0x10000, v2
	v_add_u32_e32 v170, 0x14000, v2
	v_add_u32_e32 v171, 0x18000, v2
	v_add_u32_e32 v172, 0x1c000, v2
	s_cselect_b64 s[44:45], -1, 0
	v_add_u32_e32 v173, 0x10400, v2
	v_add_u32_e32 v174, 0x10800, v2
	v_add_u32_e32 v175, 0x10c00, v2
	v_add_u32_e32 v176, 0x14400, v2
	v_add_u32_e32 v177, 0x14800, v2
	v_add_u32_e32 v178, 0x14c00, v2
	v_add_u32_e32 v179, 0x18400, v2
	v_add_u32_e32 v180, 0x18800, v2
	v_add_u32_e32 v181, 0x18c00, v2
	v_add_u32_e32 v182, 0x1c400, v2
	v_add_u32_e32 v183, 0x1c800, v2
	v_add_u32_e32 v184, 0x1cc00, v2
	v_add3_u32 v162, v6, v4, v5
	v_mov_b32_e32 v163, v161
	s_mov_b32 s87, 0
	s_mov_b32 s95, s36
	s_barrier
	v_readlane_b32 s37, v253, 46
	s_branch .LBB0_1772
